# fp8 w2 weight quantization (ph_quant_w) also deferred to the GEMM tail rounds, one 64x64 item per wave; its column-max tables moved to an unused workspace hole
# baseline (speedup 1.0000x reference)
.LBB0_39:
	v_readlane_b32 s0, v251, 5
	v_readlane_b32 s6, v251, 11
	v_readlane_b32 s7, v251, 12
	s_add_u32 s0, s6, 0x4800000
	v_readlane_b32 s1, v251, 6
	v_writelane_b32 v252, s0, 0
	s_addc_u32 s0, s7, 0
	v_writelane_b32 v252, s0, 1
	s_add_u32 s0, s6, 0x28a5c000
	v_writelane_b32 v252, s0, 2
	s_addc_u32 s0, s7, 0
	v_writelane_b32 v252, s0, 3
	s_add_u32 s0, s6, 0x289ec000
	v_writelane_b32 v252, s0, 4
	s_addc_u32 s0, s7, 0
	v_writelane_b32 v252, s0, 5
	s_add_u32 s0, s6, 0x2882c000
	v_writelane_b32 v252, s0, 6
	s_addc_u32 s0, s7, 0
	v_writelane_b32 v252, s0, 7
	s_add_u32 s0, s6, 0x28800000
	s_addc_u32 s1, s7, 0
	v_writelane_b32 v252, s0, 8
	v_readlane_b32 s2, v251, 7
	v_readlane_b32 s3, v251, 8
	v_writelane_b32 v252, s1, 9
	s_add_u32 s0, s6, 0x4820000
	v_writelane_b32 v252, s0, 10
	s_addc_u32 s0, s7, 0
	v_writelane_b32 v252, s0, 11
	s_cmpk_gt_i32 s16, 0xf5f
	v_readlane_b32 s4, v251, 9
	v_readlane_b32 s5, v251, 10
	s_cbranch_scc1 .LBB0_104
	v_mbcnt_hi_u32_b32 v0, -1, v51
	v_and_b32_e32 v3, 64, v0
	v_xor_b32_e32 v2, 16, v0
	v_add_u32_e32 v3, 64, v3
	v_cmp_lt_i32_e32 vcc, v2, v3
	s_add_i32 s20, s16, 0x26c0
	s_waitcnt lgkmcnt(1)
	v_lshrrev_b32_e32 v10, 4, v1
	v_cndmask_b32_e32 v2, v0, v2, vcc
	v_lshlrev_b32_e32 v8, 2, v2
	v_xor_b32_e32 v2, 32, v0
	v_cmp_lt_i32_e32 vcc, v2, v3
	v_cmp_gt_u32_e64 s[0:1], 16, v1
	v_mov_b32_e32 v3, 0
	v_cndmask_b32_e32 v0, v0, v2, vcc
	v_lshlrev_b32_e32 v9, 2, v0
	v_lshlrev_b32_e32 v0, 2, v1
	s_waitcnt lgkmcnt(0)
	v_and_b32_e32 v11, 60, v0
	s_branch .LBB0_42

.LBB0_309:
	s_mov_b32 s2, s0
	v_writelane_b32 v255, s2, 29
	s_cmp_lg_u32 s0, 0
	s_cselect_b64 s[0:1], -1, 0
	v_writelane_b32 v255, s3, 30
	v_writelane_b32 v255, s0, 31
	s_and_b64 vcc, exec, s[0:1]
	s_nop 0
	v_writelane_b32 v255, s1, 32
	s_branch .LBB0_380
	v_readlane_b32 s2, v251, 21
	v_readlane_b32 s3, v251, 22
	v_readlane_b32 s0, v251, 20
	s_mov_b32 s1, s2
	v_readlane_b32 s10, v251, 23
	s_waitcnt vmcnt(14)
	v_mov_b32_e32 v6, v246
	v_readlane_b32 s2, v251, 4
	v_readlane_b32 s3, v251, 2
	s_cmpk_gt_i32 s1, 0x3d7f
	s_cbranch_scc1 .LBB0_380
	v_and_b32_e32 v3, 63, v6
	v_mov_b32_e32 v1, 0x1200
	v_cmp_gt_u32_e64 s[36:37], 16, v3
	v_lshlrev_b32_e32 v3, 4, v6
	v_mul_lo_u32 v7, s0, v1
	v_bfe_u32 v1, v6, 4, 2
	v_and_b32_e32 v4, 48, v3
	v_lshlrev_b32_e32 v2, 2, v6
	v_mul_u32_u24_e32 v8, 0x44, v4
	v_mul_u32_u24_e32 v3, 0x44, v1
	s_waitcnt vmcnt(13)
	v_bfe_u32 v12, v6, 2, 4
	v_and_b32_e32 v2, 60, v2
	v_or_b32_e32 v3, v7, v3
	v_or_b32_e32 v6, v8, v12
	s_add_i32 s11, s1, 0x9b00
	v_mov_b32_e32 v5, v67
	v_add3_u32 v3, v3, v2, 0
	v_add3_u32 v13, v6, v7, 0
	v_lshlrev_b32_e32 v6, 2, v2
	v_mov_b32_e32 v7, v67

.LBB0_1028:
	v_readlane_b32 s98, v251, 3
	v_readlane_b32 s99, v255, 29
	s_cmp_lt_u32 s98, 48
	s_cbranch_scc1 .Lq_skip_M
	s_sub_i32 s98, s98, 48
	s_lshl_b32 s98, s98, 3
	v_readlane_b32 s100, v251, 20
	s_add_i32 s98, s98, s100
	s_mov_b32 s100, 0
	s_mov_b32 s101, 0
	s_cmp_eq_u32 s99, 0
	s_cselect_b32 s100, 0x0, s100
	s_cselect_b32 s101, 0x680, s101
	s_cmp_eq_u32 s99, 1
	s_cselect_b32 s100, 0x1ac0, s100
	s_cselect_b32 s101, 0x2140, s101
	s_cmp_eq_u32 s99, 2
	s_cselect_b32 s100, 0x28c0, s100
	s_cselect_b32 s101, 0x2f40, s101
	s_add_i32 s98, s98, s100
	s_cmp_ge_u32 s98, s101
	s_cbranch_scc1 .Lq_skip_M
	s_mov_b32 s100, 0x9b00
	s_cmp_lt_u32 s98, 0x2180
	s_cselect_b32 s100, 0x7f00, s100
	s_cmp_lt_u32 s98, 0x1ec0
	s_cselect_b32 s100, 0x9dc0, s100
	s_cmp_lt_u32 s98, 0x2c0
	s_cselect_b32 s100, 0x9b00, s100
	s_add_i32 s98, s98, s100
	s_mov_b32 s101, 3
	v_writelane_b32 v117, s0, 0
	v_writelane_b32 v117, s1, 1
	v_writelane_b32 v117, s2, 2
	v_writelane_b32 v117, s3, 3
	v_writelane_b32 v117, s4, 4
	v_writelane_b32 v117, s5, 5
	v_writelane_b32 v117, s6, 6
	v_writelane_b32 v117, s7, 7
	v_writelane_b32 v117, s8, 8
	v_writelane_b32 v117, s9, 9
	v_writelane_b32 v117, s10, 10
	v_writelane_b32 v117, s11, 11
	v_writelane_b32 v117, s12, 12
	v_writelane_b32 v117, s13, 13
	v_writelane_b32 v117, s14, 14
	v_writelane_b32 v117, s15, 15
	v_writelane_b32 v117, s16, 16
	v_writelane_b32 v117, s17, 17
	v_writelane_b32 v117, s18, 18
	v_writelane_b32 v117, s19, 19
	v_writelane_b32 v117, s20, 20
	v_writelane_b32 v117, s21, 21
	v_writelane_b32 v117, s22, 22
	v_writelane_b32 v117, s23, 23
	v_writelane_b32 v117, s24, 24
	v_writelane_b32 v117, s25, 25
	v_writelane_b32 v117, s26, 26
	v_writelane_b32 v117, s27, 27
	v_writelane_b32 v117, s28, 28
	v_writelane_b32 v117, s29, 29
	v_writelane_b32 v117, s30, 30
	v_writelane_b32 v117, s31, 31
	v_writelane_b32 v117, s32, 32
	v_writelane_b32 v117, s33, 33
	v_writelane_b32 v117, s34, 34
	v_writelane_b32 v117, s35, 35
	v_writelane_b32 v117, s36, 36
	v_writelane_b32 v117, s37, 37
	v_writelane_b32 v117, s38, 38
	v_writelane_b32 v117, s39, 39
	v_writelane_b32 v117, s40, 40
	v_writelane_b32 v117, s41, 41
	v_writelane_b32 v117, s42, 42
	v_writelane_b32 v117, s43, 43
	v_writelane_b32 v117, s44, 44
	v_writelane_b32 v117, s45, 45
	v_writelane_b32 v117, s46, 46
	v_writelane_b32 v117, s47, 47
	v_writelane_b32 v117, s48, 48
	v_writelane_b32 v117, s49, 49
	v_writelane_b32 v117, s50, 50
	v_writelane_b32 v117, s51, 51
	v_writelane_b32 v117, s52, 52
	v_writelane_b32 v117, s53, 53
	v_writelane_b32 v117, s54, 54
	v_writelane_b32 v117, s55, 55
	v_writelane_b32 v117, s56, 56
	v_writelane_b32 v117, s57, 57
	v_writelane_b32 v117, s58, 58
	v_writelane_b32 v117, s59, 59
	v_writelane_b32 v117, s60, 60
	v_writelane_b32 v117, s61, 61
	v_writelane_b32 v117, s62, 62
	v_writelane_b32 v117, s63, 63
	v_writelane_b32 v118, s64, 0
	v_writelane_b32 v118, s65, 1
	v_writelane_b32 v118, s66, 2
	v_writelane_b32 v118, s67, 3
	v_writelane_b32 v118, s68, 4
	v_writelane_b32 v118, s69, 5
	v_writelane_b32 v118, s70, 6
	v_writelane_b32 v118, s71, 7
	v_writelane_b32 v118, s72, 8
	v_writelane_b32 v118, s73, 9
	v_writelane_b32 v118, s74, 10
	v_writelane_b32 v118, s75, 11
	v_writelane_b32 v118, s76, 12
	v_writelane_b32 v118, s77, 13
	v_writelane_b32 v118, s78, 14
	v_writelane_b32 v118, s79, 15
	v_writelane_b32 v118, s80, 16
	v_writelane_b32 v118, s81, 17
	v_writelane_b32 v118, s82, 18
	v_writelane_b32 v118, s83, 19
	v_writelane_b32 v118, s84, 20
	v_writelane_b32 v118, s85, 21
	v_writelane_b32 v118, s86, 22
	v_writelane_b32 v118, s87, 23
	v_writelane_b32 v118, s88, 24
	v_writelane_b32 v118, s89, 25
	v_writelane_b32 v118, s90, 26
	v_writelane_b32 v118, s91, 27
	v_writelane_b32 v118, s92, 28
	v_writelane_b32 v118, s93, 29
	v_writelane_b32 v118, s94, 30
	v_writelane_b32 v118, s95, 31
	v_writelane_b32 v118, s96, 32
	v_writelane_b32 v118, s97, 33
	v_mov_b32_e32 v100, v0
	v_mov_b32_e32 v101, v50
	v_mov_b32_e32 v102, v51
	v_mov_b32_e32 v103, v52
	v_mov_b32_e32 v104, v54
	v_mov_b32_e32 v105, v55
	v_mov_b32_e32 v106, v56
	v_mov_b32_e32 v107, v58
	v_mov_b32_e32 v108, v59
	v_mov_b32_e32 v109, v60
	v_mov_b32_e32 v110, v62
	v_mov_b32_e32 v111, v63
	v_mov_b32_e32 v112, v64
	v_mov_b32_e32 v113, v67
	v_mov_b32_e32 v114, v75
	v_mov_b32_e32 v115, v77
	s_branch .Lq_entry

.Lq_skip_M:
	s_waitcnt lgkmcnt(0)
	s_barrier
	v_readlane_b32 s98, v251, 3
	v_readlane_b32 s99, v255, 29
	s_cmp_lt_u32 s98, 48
	s_cbranch_scc1 .Lwqd_skip_M
	s_sub_i32 s98, s98, 48
	s_mov_b32 s100, 0
	s_mov_b32 s101, 0
	s_cmp_eq_u32 s99, 0
	s_cselect_b32 s100, 0xe0, s100
	s_cselect_b32 s101, 0x280, s101
	s_cmp_eq_u32 s99, 1
	s_cselect_b32 s100, 0x880, s100
	s_cselect_b32 s101, 0xa20, s101
	s_cmp_eq_u32 s99, 2
	s_cselect_b32 s100, 0xc00, s100
	s_cselect_b32 s101, 0xda0, s101
	s_add_i32 s98, s98, s100
	s_mov_b32 s99, s101
	s_cmp_ge_u32 s98, s99
	s_cbranch_scc1 .Lwqd_skip_M
	s_movk_i32 s100, 208
	s_mov_b32 s101, 3
	v_writelane_b32 v117, s0, 0
	v_writelane_b32 v117, s1, 1
	v_writelane_b32 v117, s2, 2
	v_writelane_b32 v117, s3, 3
	v_writelane_b32 v117, s4, 4
	v_writelane_b32 v117, s5, 5
	v_writelane_b32 v117, s6, 6
	v_writelane_b32 v117, s7, 7
	v_writelane_b32 v117, s8, 8
	v_writelane_b32 v117, s9, 9
	v_writelane_b32 v117, s10, 10
	v_writelane_b32 v117, s11, 11
	v_writelane_b32 v117, s12, 12
	v_writelane_b32 v117, s13, 13
	v_writelane_b32 v117, s14, 14
	v_writelane_b32 v117, s15, 15
	v_writelane_b32 v117, s16, 16
	v_writelane_b32 v117, s17, 17
	v_writelane_b32 v117, s18, 18
	v_writelane_b32 v117, s19, 19
	v_writelane_b32 v117, s20, 20
	v_writelane_b32 v117, s21, 21
	v_writelane_b32 v117, s22, 22
	v_writelane_b32 v117, s23, 23
	v_writelane_b32 v117, s24, 24
	v_writelane_b32 v117, s25, 25
	v_writelane_b32 v117, s26, 26
	v_writelane_b32 v117, s27, 27
	v_writelane_b32 v117, s28, 28
	v_writelane_b32 v117, s29, 29
	v_writelane_b32 v117, s30, 30
	v_writelane_b32 v117, s31, 31
	v_writelane_b32 v117, s32, 32
	v_writelane_b32 v117, s33, 33
	v_writelane_b32 v117, s34, 34
	v_writelane_b32 v117, s35, 35
	v_writelane_b32 v117, s36, 36
	v_writelane_b32 v117, s37, 37
	v_writelane_b32 v117, s38, 38
	v_writelane_b32 v117, s39, 39
	v_writelane_b32 v117, s40, 40
	v_writelane_b32 v117, s41, 41
	v_writelane_b32 v117, s42, 42
	v_writelane_b32 v117, s43, 43
	v_writelane_b32 v117, s44, 44
	v_writelane_b32 v117, s45, 45
	v_writelane_b32 v117, s46, 46
	v_writelane_b32 v117, s47, 47
	v_writelane_b32 v117, s48, 48
	v_writelane_b32 v117, s49, 49
	v_writelane_b32 v117, s50, 50
	v_writelane_b32 v117, s51, 51
	v_writelane_b32 v117, s52, 52
	v_writelane_b32 v117, s53, 53
	v_writelane_b32 v117, s54, 54
	v_writelane_b32 v117, s55, 55
	v_writelane_b32 v117, s56, 56
	v_writelane_b32 v117, s57, 57
	v_writelane_b32 v117, s58, 58
	v_writelane_b32 v117, s59, 59
	v_writelane_b32 v117, s60, 60
	v_writelane_b32 v117, s61, 61
	v_writelane_b32 v117, s62, 62
	v_writelane_b32 v117, s63, 63
	v_writelane_b32 v118, s64, 0
	v_writelane_b32 v118, s65, 1
	v_writelane_b32 v118, s66, 2
	v_writelane_b32 v118, s67, 3
	v_writelane_b32 v118, s68, 4
	v_writelane_b32 v118, s69, 5
	v_writelane_b32 v118, s70, 6
	v_writelane_b32 v118, s71, 7
	v_writelane_b32 v118, s72, 8
	v_writelane_b32 v118, s73, 9
	v_writelane_b32 v118, s74, 10
	v_writelane_b32 v118, s75, 11
	v_writelane_b32 v118, s76, 12
	v_writelane_b32 v118, s77, 13
	v_writelane_b32 v118, s78, 14
	v_writelane_b32 v118, s79, 15
	v_writelane_b32 v118, s80, 16
	v_writelane_b32 v118, s81, 17
	v_writelane_b32 v118, s82, 18
	v_writelane_b32 v118, s83, 19
	v_writelane_b32 v118, s84, 20
	v_writelane_b32 v118, s85, 21
	v_writelane_b32 v118, s86, 22
	v_writelane_b32 v118, s87, 23
	v_writelane_b32 v118, s88, 24
	v_writelane_b32 v118, s89, 25
	v_writelane_b32 v118, s90, 26
	v_writelane_b32 v118, s91, 27
	v_writelane_b32 v118, s92, 28
	v_writelane_b32 v118, s93, 29
	v_writelane_b32 v118, s94, 30
	v_writelane_b32 v118, s95, 31
	v_writelane_b32 v118, s96, 32
	v_writelane_b32 v118, s97, 33
	v_mov_b32_e32 v100, v0
	v_mov_b32_e32 v101, v50
	v_mov_b32_e32 v102, v51
	v_mov_b32_e32 v103, v52
	v_mov_b32_e32 v104, v54
	v_mov_b32_e32 v105, v55
	v_mov_b32_e32 v106, v56
	v_mov_b32_e32 v107, v58
	v_mov_b32_e32 v108, v59
	v_mov_b32_e32 v109, v60
	v_mov_b32_e32 v110, v62
	v_mov_b32_e32 v111, v63
	v_mov_b32_e32 v112, v64
	v_mov_b32_e32 v113, v67
	v_mov_b32_e32 v114, v75
	v_mov_b32_e32 v115, v77
	s_branch .Lwqd_entry

.Lq_entry:
	s_mov_b32 s9, 0
	v_readlane_b32 s2, v251, 21
	v_readlane_b32 s3, v251, 22
	v_readlane_b32 s0, v251, 20
	s_mov_b32 s1, s2
	v_readlane_b32 s10, v251, 23
	s_waitcnt vmcnt(14)
	v_mov_b32_e32 v6, v246
	v_readlane_b32 s2, v251, 4
	v_readlane_b32 s3, v251, 2
	s_cmp_eq_u32 s98, 0
	s_cbranch_scc1 .Lq_exit
	v_and_b32_e32 v3, 63, v6
	v_mov_b32_e32 v1, 0x1200
	v_cmp_gt_u32_e64 s[36:37], 16, v3
	v_lshlrev_b32_e32 v3, 4, v6
	v_mul_lo_u32 v7, s0, v1
	v_bfe_u32 v1, v6, 4, 2
	v_and_b32_e32 v4, 48, v3
	v_lshlrev_b32_e32 v2, 2, v6
	v_mul_u32_u24_e32 v8, 0x44, v4
	v_mul_u32_u24_e32 v3, 0x44, v1
	s_waitcnt vmcnt(13)
	v_bfe_u32 v12, v6, 2, 4
	v_and_b32_e32 v2, 60, v2
	v_or_b32_e32 v3, v7, v3
	v_or_b32_e32 v6, v8, v12
	s_mov_b32 s11, s98
	v_mov_b32_e32 v5, v67
	v_add3_u32 v3, v3, v2, 0
	v_add3_u32 v13, v6, v7, 0
	v_lshlrev_b32_e32 v6, 2, v2
	v_mov_b32_e32 v7, v67

.Lq_366:
	v_add_u32_e32 v11, s1, v13
	v_add_u32_e32 v14, s1, v10
	ds_read_u8 v17, v11
	ds_read_u8 v18, v11 offset:68
	ds_read_u8 v19, v11 offset:136
	ds_read_u8 v20, v11 offset:204
	ds_read_u8 v21, v11 offset:220
	ds_read_u8 v26, v11 offset:152
	ds_read_u8 v27, v11 offset:84
	ds_read_u8 v28, v11 offset:16
	ds_read_u8 v29, v11 offset:272
	ds_read_u8 v30, v11 offset:340
	ds_read_u8 v31, v11 offset:408
	ds_read_u8 v32, v11 offset:476
	ds_read_u8 v33, v11 offset:492
	ds_read_u8 v34, v11 offset:424
	ds_read_u8 v35, v11 offset:356
	ds_read_u8 v36, v11 offset:288
	ds_read_u8 v37, v11 offset:544
	ds_read_u8 v38, v11 offset:612
	ds_read_u8 v39, v11 offset:680
	ds_read_u8 v40, v11 offset:748
	ds_read_u8 v41, v11 offset:764
	ds_read_u8 v42, v11 offset:696
	ds_read_u8 v43, v11 offset:628
	ds_read_u8 v44, v11 offset:560
	ds_read_u8 v45, v11 offset:816
	ds_read_u8 v46, v11 offset:884
	ds_read_u8 v47, v11 offset:952
	ds_read_u8 v48, v11 offset:1020
	ds_read_u8 v49, v11 offset:1036
	ds_read_u8 v50, v11 offset:968
	ds_read_u8 v51, v11 offset:900
	ds_read_u8 v11, v11 offset:832
	v_ashrrev_i32_e32 v15, 31, v14
	v_mul_lo_u32 v16, s39, v14
	v_mad_u64_u32 v[22:23], s[2:3], s38, v14, v[8:9]
	v_add_u32_e32 v14, 16, v14
	v_ashrrev_i32_e32 v52, 31, v14
	v_mul_lo_u32 v15, s38, v15
	v_mul_lo_u32 v53, s39, v14
	v_mad_u64_u32 v[24:25], s[2:3], s38, v14, v[8:9]
	v_mul_lo_u32 v14, s38, v52
	s_add_i32 s1, s1, 32
	v_add3_u32 v23, v16, v23, v15
	v_add3_u32 v25, v53, v25, v14
	s_waitcnt lgkmcnt(14)
	v_lshl_or_b32 v14, v18, 8, v17
	v_lshlrev_b32_e32 v15, 16, v19
	v_lshlrev_b32_e32 v16, 24, v20
	v_lshl_or_b32 v17, v30, 8, v29
	v_lshlrev_b32_e32 v18, 16, v31
	v_lshlrev_b32_e32 v19, 24, v32
	v_lshl_or_b32 v20, v38, 8, v37
	s_waitcnt lgkmcnt(13)
	v_lshlrev_b32_e32 v29, 16, v39
	s_waitcnt lgkmcnt(12)
	v_lshlrev_b32_e32 v30, 24, v40
	s_waitcnt lgkmcnt(6)
	v_lshl_or_b32 v31, v46, 8, v45
	s_waitcnt lgkmcnt(5)
	v_lshlrev_b32_e32 v32, 16, v47
	s_waitcnt lgkmcnt(4)
	v_lshlrev_b32_e32 v37, 24, v48
	s_cmp_eq_u32 s1, 64
	v_lshl_or_b32 v27, v27, 8, v28
	v_lshlrev_b32_e32 v26, 16, v26
	v_lshlrev_b32_e32 v21, 24, v21
	v_lshl_or_b32 v28, v35, 8, v36
	v_lshlrev_b32_e32 v34, 16, v34
	v_lshlrev_b32_e32 v33, 24, v33
	v_lshl_or_b32 v35, v43, 8, v44
	v_lshlrev_b32_e32 v36, 16, v42
	v_lshlrev_b32_e32 v38, 24, v41
	s_waitcnt lgkmcnt(0)
	v_lshl_or_b32 v11, v51, 8, v11
	v_lshlrev_b32_e32 v39, 16, v50
	v_lshlrev_b32_e32 v40, 24, v49
	v_or3_b32 v14, v14, v15, v16
	v_or3_b32 v15, v17, v18, v19
	v_or3_b32 v16, v20, v29, v30
	v_or3_b32 v17, v31, v32, v37
	v_or3_b32 v18, v27, v26, v21
	v_or3_b32 v19, v28, v34, v33
	v_or3_b32 v20, v35, v36, v38
	v_or3_b32 v21, v11, v39, v40
	global_store_dwordx4 v[22:23], v[14:17], off
	global_store_dwordx4 v[24:25], v[18:21], off
	s_cbranch_scc0 .Lq_366
	s_waitcnt lgkmcnt(0)
	s_add_i32 s11, s11, s10
	s_cmp_gt_i32 s11, 0xd87f
	s_nop 0
	s_branch .Lq_exit

.LBB0_1159:
	v_readlane_b32 s98, v251, 3
	v_readlane_b32 s99, v255, 29
	s_cmp_lt_u32 s98, 16
	s_cbranch_scc1 .Lq_skip_A
	s_sub_i32 s98, s98, 16
	s_lshl_b32 s98, s98, 3
	v_readlane_b32 s100, v251, 20
	s_add_i32 s98, s98, s100
	s_mov_b32 s100, 0
	s_mov_b32 s101, 0
	s_cmp_eq_u32 s99, 0
	s_cselect_b32 s100, 0x680, s100
	s_cselect_b32 s101, 0xe00, s101
	s_cmp_eq_u32 s99, 1
	s_cselect_b32 s100, 0x2140, s100
	s_cselect_b32 s101, 0x28c0, s101
	s_cmp_eq_u32 s99, 2
	s_cselect_b32 s100, 0x2f40, s100
	s_cselect_b32 s101, 0x36c0, s101
	s_add_i32 s98, s98, s100
	s_cmp_ge_u32 s98, s101
	s_cbranch_scc1 .Lq_skip_A
	s_mov_b32 s100, 0x9b00
	s_cmp_lt_u32 s98, 0x2180
	s_cselect_b32 s100, 0x7f00, s100
	s_cmp_lt_u32 s98, 0x1ec0
	s_cselect_b32 s100, 0x9dc0, s100
	s_cmp_lt_u32 s98, 0x2c0
	s_cselect_b32 s100, 0x9b00, s100
	s_add_i32 s98, s98, s100
	s_mov_b32 s101, 1
	v_writelane_b32 v117, s0, 0
	v_writelane_b32 v117, s1, 1
	v_writelane_b32 v117, s2, 2
	v_writelane_b32 v117, s3, 3
	v_writelane_b32 v117, s4, 4
	v_writelane_b32 v117, s5, 5
	v_writelane_b32 v117, s6, 6
	v_writelane_b32 v117, s7, 7
	v_writelane_b32 v117, s8, 8
	v_writelane_b32 v117, s9, 9
	v_writelane_b32 v117, s10, 10
	v_writelane_b32 v117, s11, 11
	v_writelane_b32 v117, s12, 12
	v_writelane_b32 v117, s13, 13
	v_writelane_b32 v117, s14, 14
	v_writelane_b32 v117, s15, 15
	v_writelane_b32 v117, s16, 16
	v_writelane_b32 v117, s17, 17
	v_writelane_b32 v117, s18, 18
	v_writelane_b32 v117, s19, 19
	v_writelane_b32 v117, s20, 20
	v_writelane_b32 v117, s21, 21
	v_writelane_b32 v117, s22, 22
	v_writelane_b32 v117, s23, 23
	v_writelane_b32 v117, s24, 24
	v_writelane_b32 v117, s25, 25
	v_writelane_b32 v117, s26, 26
	v_writelane_b32 v117, s27, 27
	v_writelane_b32 v117, s28, 28
	v_writelane_b32 v117, s29, 29
	v_writelane_b32 v117, s30, 30
	v_writelane_b32 v117, s31, 31
	v_writelane_b32 v117, s32, 32
	v_writelane_b32 v117, s33, 33
	v_writelane_b32 v117, s34, 34
	v_writelane_b32 v117, s35, 35
	v_writelane_b32 v117, s36, 36
	v_writelane_b32 v117, s37, 37
	v_writelane_b32 v117, s38, 38
	v_writelane_b32 v117, s39, 39
	v_writelane_b32 v117, s40, 40
	v_writelane_b32 v117, s41, 41
	v_writelane_b32 v117, s42, 42
	v_writelane_b32 v117, s43, 43
	v_writelane_b32 v117, s44, 44
	v_writelane_b32 v117, s45, 45
	v_writelane_b32 v117, s46, 46
	v_writelane_b32 v117, s47, 47
	v_writelane_b32 v117, s48, 48
	v_writelane_b32 v117, s49, 49
	v_writelane_b32 v117, s50, 50
	v_writelane_b32 v117, s51, 51
	v_writelane_b32 v117, s52, 52
	v_writelane_b32 v117, s53, 53
	v_writelane_b32 v117, s54, 54
	v_writelane_b32 v117, s55, 55
	v_writelane_b32 v117, s56, 56
	v_writelane_b32 v117, s57, 57
	v_writelane_b32 v117, s58, 58
	v_writelane_b32 v117, s59, 59
	v_writelane_b32 v117, s60, 60
	v_writelane_b32 v117, s61, 61
	v_writelane_b32 v117, s62, 62
	v_writelane_b32 v117, s63, 63
	v_writelane_b32 v118, s64, 0
	v_writelane_b32 v118, s65, 1
	v_writelane_b32 v118, s66, 2
	v_writelane_b32 v118, s67, 3
	v_writelane_b32 v118, s68, 4
	v_writelane_b32 v118, s69, 5
	v_writelane_b32 v118, s70, 6
	v_writelane_b32 v118, s71, 7
	v_writelane_b32 v118, s72, 8
	v_writelane_b32 v118, s73, 9
	v_writelane_b32 v118, s74, 10
	v_writelane_b32 v118, s75, 11
	v_writelane_b32 v118, s76, 12
	v_writelane_b32 v118, s77, 13
	v_writelane_b32 v118, s78, 14
	v_writelane_b32 v118, s79, 15
	v_writelane_b32 v118, s80, 16
	v_writelane_b32 v118, s81, 17
	v_writelane_b32 v118, s82, 18
	v_writelane_b32 v118, s83, 19
	v_writelane_b32 v118, s84, 20
	v_writelane_b32 v118, s85, 21
	v_writelane_b32 v118, s86, 22
	v_writelane_b32 v118, s87, 23
	v_writelane_b32 v118, s88, 24
	v_writelane_b32 v118, s89, 25
	v_writelane_b32 v118, s90, 26
	v_writelane_b32 v118, s91, 27
	v_writelane_b32 v118, s92, 28
	v_writelane_b32 v118, s93, 29
	v_writelane_b32 v118, s94, 30
	v_writelane_b32 v118, s95, 31
	v_writelane_b32 v118, s96, 32
	v_writelane_b32 v118, s97, 33
	v_mov_b32_e32 v100, v0
	v_mov_b32_e32 v101, v50
	v_mov_b32_e32 v102, v51
	v_mov_b32_e32 v103, v52
	v_mov_b32_e32 v104, v54
	v_mov_b32_e32 v105, v55
	v_mov_b32_e32 v106, v56
	v_mov_b32_e32 v107, v58
	v_mov_b32_e32 v108, v59
	v_mov_b32_e32 v109, v60
	v_mov_b32_e32 v110, v62
	v_mov_b32_e32 v111, v63
	v_mov_b32_e32 v112, v64
	v_mov_b32_e32 v113, v67
	v_mov_b32_e32 v114, v75
	v_mov_b32_e32 v115, v77
	s_branch .Lq_entry

.Lq_skip_A:
	s_waitcnt lgkmcnt(0)
	s_barrier
	v_readlane_b32 s98, v251, 3
	v_readlane_b32 s99, v255, 29
	s_cmp_lt_u32 s98, 16
	s_cbranch_scc1 .Lwqd_skip_A
	s_sub_i32 s98, s98, 16
	s_mov_b32 s100, 0
	s_mov_b32 s101, 0
	s_cmp_eq_u32 s99, 0
	s_cselect_b32 s100, 0x280, s100
	s_cselect_b32 s101, 0x460, s101
	s_cmp_eq_u32 s99, 1
	s_cselect_b32 s100, 0xa20, s100
	s_cselect_b32 s101, 0xc00, s101
	s_cmp_eq_u32 s99, 2
	s_cselect_b32 s100, 0xda0, s100
	s_cselect_b32 s101, 0xf80, s101
	s_add_i32 s98, s98, s100
	s_mov_b32 s99, s101
	s_cmp_ge_u32 s98, s99
	s_cbranch_scc1 .Lwqd_skip_A
	s_movk_i32 s100, 240
	s_mov_b32 s101, 1
	v_writelane_b32 v117, s0, 0
	v_writelane_b32 v117, s1, 1
	v_writelane_b32 v117, s2, 2
	v_writelane_b32 v117, s3, 3
	v_writelane_b32 v117, s4, 4
	v_writelane_b32 v117, s5, 5
	v_writelane_b32 v117, s6, 6
	v_writelane_b32 v117, s7, 7
	v_writelane_b32 v117, s8, 8
	v_writelane_b32 v117, s9, 9
	v_writelane_b32 v117, s10, 10
	v_writelane_b32 v117, s11, 11
	v_writelane_b32 v117, s12, 12
	v_writelane_b32 v117, s13, 13
	v_writelane_b32 v117, s14, 14
	v_writelane_b32 v117, s15, 15
	v_writelane_b32 v117, s16, 16
	v_writelane_b32 v117, s17, 17
	v_writelane_b32 v117, s18, 18
	v_writelane_b32 v117, s19, 19
	v_writelane_b32 v117, s20, 20
	v_writelane_b32 v117, s21, 21
	v_writelane_b32 v117, s22, 22
	v_writelane_b32 v117, s23, 23
	v_writelane_b32 v117, s24, 24
	v_writelane_b32 v117, s25, 25
	v_writelane_b32 v117, s26, 26
	v_writelane_b32 v117, s27, 27
	v_writelane_b32 v117, s28, 28
	v_writelane_b32 v117, s29, 29
	v_writelane_b32 v117, s30, 30
	v_writelane_b32 v117, s31, 31
	v_writelane_b32 v117, s32, 32
	v_writelane_b32 v117, s33, 33
	v_writelane_b32 v117, s34, 34
	v_writelane_b32 v117, s35, 35
	v_writelane_b32 v117, s36, 36
	v_writelane_b32 v117, s37, 37
	v_writelane_b32 v117, s38, 38
	v_writelane_b32 v117, s39, 39
	v_writelane_b32 v117, s40, 40
	v_writelane_b32 v117, s41, 41
	v_writelane_b32 v117, s42, 42
	v_writelane_b32 v117, s43, 43
	v_writelane_b32 v117, s44, 44
	v_writelane_b32 v117, s45, 45
	v_writelane_b32 v117, s46, 46
	v_writelane_b32 v117, s47, 47
	v_writelane_b32 v117, s48, 48
	v_writelane_b32 v117, s49, 49
	v_writelane_b32 v117, s50, 50
	v_writelane_b32 v117, s51, 51
	v_writelane_b32 v117, s52, 52
	v_writelane_b32 v117, s53, 53
	v_writelane_b32 v117, s54, 54
	v_writelane_b32 v117, s55, 55
	v_writelane_b32 v117, s56, 56
	v_writelane_b32 v117, s57, 57
	v_writelane_b32 v117, s58, 58
	v_writelane_b32 v117, s59, 59
	v_writelane_b32 v117, s60, 60
	v_writelane_b32 v117, s61, 61
	v_writelane_b32 v117, s62, 62
	v_writelane_b32 v117, s63, 63
	v_writelane_b32 v118, s64, 0
	v_writelane_b32 v118, s65, 1
	v_writelane_b32 v118, s66, 2
	v_writelane_b32 v118, s67, 3
	v_writelane_b32 v118, s68, 4
	v_writelane_b32 v118, s69, 5
	v_writelane_b32 v118, s70, 6
	v_writelane_b32 v118, s71, 7
	v_writelane_b32 v118, s72, 8
	v_writelane_b32 v118, s73, 9
	v_writelane_b32 v118, s74, 10
	v_writelane_b32 v118, s75, 11
	v_writelane_b32 v118, s76, 12
	v_writelane_b32 v118, s77, 13
	v_writelane_b32 v118, s78, 14
	v_writelane_b32 v118, s79, 15
	v_writelane_b32 v118, s80, 16
	v_writelane_b32 v118, s81, 17
	v_writelane_b32 v118, s82, 18
	v_writelane_b32 v118, s83, 19
	v_writelane_b32 v118, s84, 20
	v_writelane_b32 v118, s85, 21
	v_writelane_b32 v118, s86, 22
	v_writelane_b32 v118, s87, 23
	v_writelane_b32 v118, s88, 24
	v_writelane_b32 v118, s89, 25
	v_writelane_b32 v118, s90, 26
	v_writelane_b32 v118, s91, 27
	v_writelane_b32 v118, s92, 28
	v_writelane_b32 v118, s93, 29
	v_writelane_b32 v118, s94, 30
	v_writelane_b32 v118, s95, 31
	v_writelane_b32 v118, s96, 32
	v_writelane_b32 v118, s97, 33
	v_mov_b32_e32 v100, v0
	v_mov_b32_e32 v101, v50
	v_mov_b32_e32 v102, v51
	v_mov_b32_e32 v103, v52
	v_mov_b32_e32 v104, v54
	v_mov_b32_e32 v105, v55
	v_mov_b32_e32 v106, v56
	v_mov_b32_e32 v107, v58
	v_mov_b32_e32 v108, v59
	v_mov_b32_e32 v109, v60
	v_mov_b32_e32 v110, v62
	v_mov_b32_e32 v111, v63
	v_mov_b32_e32 v112, v64
	v_mov_b32_e32 v113, v67
	v_mov_b32_e32 v114, v75
	v_mov_b32_e32 v115, v77
	s_branch .Lwqd_entry

.LBB0_1699:
	v_readlane_b32 s98, v251, 3
	v_readlane_b32 s99, v255, 29
	s_cmp_lt_u32 s98, 88
	s_cbranch_scc1 .Lq_skip_G
	s_sub_i32 s98, s98, 88
	s_lshl_b32 s98, s98, 3
	v_readlane_b32 s100, v251, 20
	s_add_i32 s98, s98, s100
	s_mov_b32 s100, 0
	s_mov_b32 s101, 0
	s_cmp_eq_u32 s99, 0
	s_cselect_b32 s100, 0xe00, s100
	s_cselect_b32 s101, 0x1340, s101
	s_cmp_eq_u32 s99, 2
	s_cselect_b32 s100, 0x36c0, s100
	s_cselect_b32 s101, 0x3c00, s101
	s_add_i32 s98, s98, s100
	s_cmp_ge_u32 s98, s101
	s_cbranch_scc1 .Lq_skip_G
	s_mov_b32 s100, 0x9b00
	s_cmp_lt_u32 s98, 0x2180
	s_cselect_b32 s100, 0x7f00, s100
	s_cmp_lt_u32 s98, 0x1ec0
	s_cselect_b32 s100, 0x9dc0, s100
	s_cmp_lt_u32 s98, 0x2c0
	s_cselect_b32 s100, 0x9b00, s100
	s_add_i32 s98, s98, s100
	s_mov_b32 s101, 4
	v_writelane_b32 v117, s0, 0
	v_writelane_b32 v117, s1, 1
	v_writelane_b32 v117, s2, 2
	v_writelane_b32 v117, s3, 3
	v_writelane_b32 v117, s4, 4
	v_writelane_b32 v117, s5, 5
	v_writelane_b32 v117, s6, 6
	v_writelane_b32 v117, s7, 7
	v_writelane_b32 v117, s8, 8
	v_writelane_b32 v117, s9, 9
	v_writelane_b32 v117, s10, 10
	v_writelane_b32 v117, s11, 11
	v_writelane_b32 v117, s12, 12
	v_writelane_b32 v117, s13, 13
	v_writelane_b32 v117, s14, 14
	v_writelane_b32 v117, s15, 15
	v_writelane_b32 v117, s16, 16
	v_writelane_b32 v117, s17, 17
	v_writelane_b32 v117, s18, 18
	v_writelane_b32 v117, s19, 19
	v_writelane_b32 v117, s20, 20
	v_writelane_b32 v117, s21, 21
	v_writelane_b32 v117, s22, 22
	v_writelane_b32 v117, s23, 23
	v_writelane_b32 v117, s24, 24
	v_writelane_b32 v117, s25, 25
	v_writelane_b32 v117, s26, 26
	v_writelane_b32 v117, s27, 27
	v_writelane_b32 v117, s28, 28
	v_writelane_b32 v117, s29, 29
	v_writelane_b32 v117, s30, 30
	v_writelane_b32 v117, s31, 31
	v_writelane_b32 v117, s32, 32
	v_writelane_b32 v117, s33, 33
	v_writelane_b32 v117, s34, 34
	v_writelane_b32 v117, s35, 35
	v_writelane_b32 v117, s36, 36
	v_writelane_b32 v117, s37, 37
	v_writelane_b32 v117, s38, 38
	v_writelane_b32 v117, s39, 39
	v_writelane_b32 v117, s40, 40
	v_writelane_b32 v117, s41, 41
	v_writelane_b32 v117, s42, 42
	v_writelane_b32 v117, s43, 43
	v_writelane_b32 v117, s44, 44
	v_writelane_b32 v117, s45, 45
	v_writelane_b32 v117, s46, 46
	v_writelane_b32 v117, s47, 47
	v_writelane_b32 v117, s48, 48
	v_writelane_b32 v117, s49, 49
	v_writelane_b32 v117, s50, 50
	v_writelane_b32 v117, s51, 51
	v_writelane_b32 v117, s52, 52
	v_writelane_b32 v117, s53, 53
	v_writelane_b32 v117, s54, 54
	v_writelane_b32 v117, s55, 55
	v_writelane_b32 v117, s56, 56
	v_writelane_b32 v117, s57, 57
	v_writelane_b32 v117, s58, 58
	v_writelane_b32 v117, s59, 59
	v_writelane_b32 v117, s60, 60
	v_writelane_b32 v117, s61, 61
	v_writelane_b32 v117, s62, 62
	v_writelane_b32 v117, s63, 63
	v_writelane_b32 v118, s64, 0
	v_writelane_b32 v118, s65, 1
	v_writelane_b32 v118, s66, 2
	v_writelane_b32 v118, s67, 3
	v_writelane_b32 v118, s68, 4
	v_writelane_b32 v118, s69, 5
	v_writelane_b32 v118, s70, 6
	v_writelane_b32 v118, s71, 7
	v_writelane_b32 v118, s72, 8
	v_writelane_b32 v118, s73, 9
	v_writelane_b32 v118, s74, 10
	v_writelane_b32 v118, s75, 11
	v_writelane_b32 v118, s76, 12
	v_writelane_b32 v118, s77, 13
	v_writelane_b32 v118, s78, 14
	v_writelane_b32 v118, s79, 15
	v_writelane_b32 v118, s80, 16
	v_writelane_b32 v118, s81, 17
	v_writelane_b32 v118, s82, 18
	v_writelane_b32 v118, s83, 19
	v_writelane_b32 v118, s84, 20
	v_writelane_b32 v118, s85, 21
	v_writelane_b32 v118, s86, 22
	v_writelane_b32 v118, s87, 23
	v_writelane_b32 v118, s88, 24
	v_writelane_b32 v118, s89, 25
	v_writelane_b32 v118, s90, 26
	v_writelane_b32 v118, s91, 27
	v_writelane_b32 v118, s92, 28
	v_writelane_b32 v118, s93, 29
	v_writelane_b32 v118, s94, 30
	v_writelane_b32 v118, s95, 31
	v_writelane_b32 v118, s96, 32
	v_writelane_b32 v118, s97, 33
	v_mov_b32_e32 v100, v0
	v_mov_b32_e32 v101, v50
	v_mov_b32_e32 v102, v51
	v_mov_b32_e32 v103, v52
	v_mov_b32_e32 v104, v54
	v_mov_b32_e32 v105, v55
	v_mov_b32_e32 v106, v56
	v_mov_b32_e32 v107, v58
	v_mov_b32_e32 v108, v59
	v_mov_b32_e32 v109, v60
	v_mov_b32_e32 v110, v62
	v_mov_b32_e32 v111, v63
	v_mov_b32_e32 v112, v64
	v_mov_b32_e32 v113, v67
	v_mov_b32_e32 v114, v75
	v_mov_b32_e32 v115, v77
	s_branch .Lq_entry

.Lq_skip_G:
	s_waitcnt lgkmcnt(0)
	s_barrier
	v_readlane_b32 s98, v251, 3
	v_readlane_b32 s99, v255, 29
	s_cmp_lt_u32 s98, 88
	s_cbranch_scc1 .Lwqd_skip_G
	s_sub_i32 s98, s98, 88
	s_mov_b32 s100, 0
	s_mov_b32 s101, 0
	s_cmp_eq_u32 s99, 0
	s_cselect_b32 s100, 0x460, s100
	s_cselect_b32 s101, 0x5b0, s101
	s_cmp_eq_u32 s99, 2
	s_cselect_b32 s100, 0xf80, s100
	s_cselect_b32 s101, 0x10d0, s101
	s_add_i32 s98, s98, s100
	s_mov_b32 s99, s101
	s_cmp_ge_u32 s98, s99
	s_cbranch_scc1 .Lwqd_skip_G
	s_movk_i32 s100, 168
	s_mov_b32 s101, 4
	v_writelane_b32 v117, s0, 0
	v_writelane_b32 v117, s1, 1
	v_writelane_b32 v117, s2, 2
	v_writelane_b32 v117, s3, 3
	v_writelane_b32 v117, s4, 4
	v_writelane_b32 v117, s5, 5
	v_writelane_b32 v117, s6, 6
	v_writelane_b32 v117, s7, 7
	v_writelane_b32 v117, s8, 8
	v_writelane_b32 v117, s9, 9
	v_writelane_b32 v117, s10, 10
	v_writelane_b32 v117, s11, 11
	v_writelane_b32 v117, s12, 12
	v_writelane_b32 v117, s13, 13
	v_writelane_b32 v117, s14, 14
	v_writelane_b32 v117, s15, 15
	v_writelane_b32 v117, s16, 16
	v_writelane_b32 v117, s17, 17
	v_writelane_b32 v117, s18, 18
	v_writelane_b32 v117, s19, 19
	v_writelane_b32 v117, s20, 20
	v_writelane_b32 v117, s21, 21
	v_writelane_b32 v117, s22, 22
	v_writelane_b32 v117, s23, 23
	v_writelane_b32 v117, s24, 24
	v_writelane_b32 v117, s25, 25
	v_writelane_b32 v117, s26, 26
	v_writelane_b32 v117, s27, 27
	v_writelane_b32 v117, s28, 28
	v_writelane_b32 v117, s29, 29
	v_writelane_b32 v117, s30, 30
	v_writelane_b32 v117, s31, 31
	v_writelane_b32 v117, s32, 32
	v_writelane_b32 v117, s33, 33
	v_writelane_b32 v117, s34, 34
	v_writelane_b32 v117, s35, 35
	v_writelane_b32 v117, s36, 36
	v_writelane_b32 v117, s37, 37
	v_writelane_b32 v117, s38, 38
	v_writelane_b32 v117, s39, 39
	v_writelane_b32 v117, s40, 40
	v_writelane_b32 v117, s41, 41
	v_writelane_b32 v117, s42, 42
	v_writelane_b32 v117, s43, 43
	v_writelane_b32 v117, s44, 44
	v_writelane_b32 v117, s45, 45
	v_writelane_b32 v117, s46, 46
	v_writelane_b32 v117, s47, 47
	v_writelane_b32 v117, s48, 48
	v_writelane_b32 v117, s49, 49
	v_writelane_b32 v117, s50, 50
	v_writelane_b32 v117, s51, 51
	v_writelane_b32 v117, s52, 52
	v_writelane_b32 v117, s53, 53
	v_writelane_b32 v117, s54, 54
	v_writelane_b32 v117, s55, 55
	v_writelane_b32 v117, s56, 56
	v_writelane_b32 v117, s57, 57
	v_writelane_b32 v117, s58, 58
	v_writelane_b32 v117, s59, 59
	v_writelane_b32 v117, s60, 60
	v_writelane_b32 v117, s61, 61
	v_writelane_b32 v117, s62, 62
	v_writelane_b32 v117, s63, 63
	v_writelane_b32 v118, s64, 0
	v_writelane_b32 v118, s65, 1
	v_writelane_b32 v118, s66, 2
	v_writelane_b32 v118, s67, 3
	v_writelane_b32 v118, s68, 4
	v_writelane_b32 v118, s69, 5
	v_writelane_b32 v118, s70, 6
	v_writelane_b32 v118, s71, 7
	v_writelane_b32 v118, s72, 8
	v_writelane_b32 v118, s73, 9
	v_writelane_b32 v118, s74, 10
	v_writelane_b32 v118, s75, 11
	v_writelane_b32 v118, s76, 12
	v_writelane_b32 v118, s77, 13
	v_writelane_b32 v118, s78, 14
	v_writelane_b32 v118, s79, 15
	v_writelane_b32 v118, s80, 16
	v_writelane_b32 v118, s81, 17
	v_writelane_b32 v118, s82, 18
	v_writelane_b32 v118, s83, 19
	v_writelane_b32 v118, s84, 20
	v_writelane_b32 v118, s85, 21
	v_writelane_b32 v118, s86, 22
	v_writelane_b32 v118, s87, 23
	v_writelane_b32 v118, s88, 24
	v_writelane_b32 v118, s89, 25
	v_writelane_b32 v118, s90, 26
	v_writelane_b32 v118, s91, 27
	v_writelane_b32 v118, s92, 28
	v_writelane_b32 v118, s93, 29
	v_writelane_b32 v118, s94, 30
	v_writelane_b32 v118, s95, 31
	v_writelane_b32 v118, s96, 32
	v_writelane_b32 v118, s97, 33
	v_mov_b32_e32 v100, v0
	v_mov_b32_e32 v101, v50
	v_mov_b32_e32 v102, v51
	v_mov_b32_e32 v103, v52
	v_mov_b32_e32 v104, v54
	v_mov_b32_e32 v105, v55
	v_mov_b32_e32 v106, v56
	v_mov_b32_e32 v107, v58
	v_mov_b32_e32 v108, v59
	v_mov_b32_e32 v109, v60
	v_mov_b32_e32 v110, v62
	v_mov_b32_e32 v111, v63
	v_mov_b32_e32 v112, v64
	v_mov_b32_e32 v113, v67
	v_mov_b32_e32 v114, v75
	v_mov_b32_e32 v115, v77
	s_branch .Lwqd_entry

.LBB0_1774:
	v_readlane_b32 s98, v251, 3
	v_readlane_b32 s99, v255, 29
	s_cmp_lt_u32 s98, 16
	s_cbranch_scc1 .Lq_skip_F
	s_sub_i32 s98, s98, 16
	s_lshl_b32 s98, s98, 3
	v_readlane_b32 s100, v251, 20
	s_add_i32 s98, s98, s100
	s_mov_b32 s100, 0
	s_mov_b32 s101, 0
	s_cmp_eq_u32 s99, 0
	s_cselect_b32 s100, 0x1340, s100
	s_cselect_b32 s101, 0x1ac0, s101
	s_cmp_eq_u32 s99, 2
	s_cselect_b32 s100, 0x3c00, s100
	s_cselect_b32 s101, 0x3d80, s101
	s_add_i32 s98, s98, s100
	s_cmp_ge_u32 s98, s101
	s_cbranch_scc1 .Lq_skip_F
	s_mov_b32 s100, 0x9b00
	s_cmp_lt_u32 s98, 0x2180
	s_cselect_b32 s100, 0x7f00, s100
	s_cmp_lt_u32 s98, 0x1ec0
	s_cselect_b32 s100, 0x9dc0, s100
	s_cmp_lt_u32 s98, 0x2c0
	s_cselect_b32 s100, 0x9b00, s100
	s_add_i32 s98, s98, s100
	s_mov_b32 s101, 2
	v_writelane_b32 v117, s0, 0
	v_writelane_b32 v117, s1, 1
	v_writelane_b32 v117, s2, 2
	v_writelane_b32 v117, s3, 3
	v_writelane_b32 v117, s4, 4
	v_writelane_b32 v117, s5, 5
	v_writelane_b32 v117, s6, 6
	v_writelane_b32 v117, s7, 7
	v_writelane_b32 v117, s8, 8
	v_writelane_b32 v117, s9, 9
	v_writelane_b32 v117, s10, 10
	v_writelane_b32 v117, s11, 11
	v_writelane_b32 v117, s12, 12
	v_writelane_b32 v117, s13, 13
	v_writelane_b32 v117, s14, 14
	v_writelane_b32 v117, s15, 15
	v_writelane_b32 v117, s16, 16
	v_writelane_b32 v117, s17, 17
	v_writelane_b32 v117, s18, 18
	v_writelane_b32 v117, s19, 19
	v_writelane_b32 v117, s20, 20
	v_writelane_b32 v117, s21, 21
	v_writelane_b32 v117, s22, 22
	v_writelane_b32 v117, s23, 23
	v_writelane_b32 v117, s24, 24
	v_writelane_b32 v117, s25, 25
	v_writelane_b32 v117, s26, 26
	v_writelane_b32 v117, s27, 27
	v_writelane_b32 v117, s28, 28
	v_writelane_b32 v117, s29, 29
	v_writelane_b32 v117, s30, 30
	v_writelane_b32 v117, s31, 31
	v_writelane_b32 v117, s32, 32
	v_writelane_b32 v117, s33, 33
	v_writelane_b32 v117, s34, 34
	v_writelane_b32 v117, s35, 35
	v_writelane_b32 v117, s36, 36
	v_writelane_b32 v117, s37, 37
	v_writelane_b32 v117, s38, 38
	v_writelane_b32 v117, s39, 39
	v_writelane_b32 v117, s40, 40
	v_writelane_b32 v117, s41, 41
	v_writelane_b32 v117, s42, 42
	v_writelane_b32 v117, s43, 43
	v_writelane_b32 v117, s44, 44
	v_writelane_b32 v117, s45, 45
	v_writelane_b32 v117, s46, 46
	v_writelane_b32 v117, s47, 47
	v_writelane_b32 v117, s48, 48
	v_writelane_b32 v117, s49, 49
	v_writelane_b32 v117, s50, 50
	v_writelane_b32 v117, s51, 51
	v_writelane_b32 v117, s52, 52
	v_writelane_b32 v117, s53, 53
	v_writelane_b32 v117, s54, 54
	v_writelane_b32 v117, s55, 55
	v_writelane_b32 v117, s56, 56
	v_writelane_b32 v117, s57, 57
	v_writelane_b32 v117, s58, 58
	v_writelane_b32 v117, s59, 59
	v_writelane_b32 v117, s60, 60
	v_writelane_b32 v117, s61, 61
	v_writelane_b32 v117, s62, 62
	v_writelane_b32 v117, s63, 63
	v_writelane_b32 v118, s64, 0
	v_writelane_b32 v118, s65, 1
	v_writelane_b32 v118, s66, 2
	v_writelane_b32 v118, s67, 3
	v_writelane_b32 v118, s68, 4
	v_writelane_b32 v118, s69, 5
	v_writelane_b32 v118, s70, 6
	v_writelane_b32 v118, s71, 7
	v_writelane_b32 v118, s72, 8
	v_writelane_b32 v118, s73, 9
	v_writelane_b32 v118, s74, 10
	v_writelane_b32 v118, s75, 11
	v_writelane_b32 v118, s76, 12
	v_writelane_b32 v118, s77, 13
	v_writelane_b32 v118, s78, 14
	v_writelane_b32 v118, s79, 15
	v_writelane_b32 v118, s80, 16
	v_writelane_b32 v118, s81, 17
	v_writelane_b32 v118, s82, 18
	v_writelane_b32 v118, s83, 19
	v_writelane_b32 v118, s84, 20
	v_writelane_b32 v118, s85, 21
	v_writelane_b32 v118, s86, 22
	v_writelane_b32 v118, s87, 23
	v_writelane_b32 v118, s88, 24
	v_writelane_b32 v118, s89, 25
	v_writelane_b32 v118, s90, 26
	v_writelane_b32 v118, s91, 27
	v_writelane_b32 v118, s92, 28
	v_writelane_b32 v118, s93, 29
	v_writelane_b32 v118, s94, 30
	v_writelane_b32 v118, s95, 31
	v_writelane_b32 v118, s96, 32
	v_writelane_b32 v118, s97, 33
	v_mov_b32_e32 v100, v0
	v_mov_b32_e32 v101, v50
	v_mov_b32_e32 v102, v51
	v_mov_b32_e32 v103, v52
	v_mov_b32_e32 v104, v54
	v_mov_b32_e32 v105, v55
	v_mov_b32_e32 v106, v56
	v_mov_b32_e32 v107, v58
	v_mov_b32_e32 v108, v59
	v_mov_b32_e32 v109, v60
	v_mov_b32_e32 v110, v62
	v_mov_b32_e32 v111, v63
	v_mov_b32_e32 v112, v64
	v_mov_b32_e32 v113, v67
	v_mov_b32_e32 v114, v75
	v_mov_b32_e32 v115, v77
	s_branch .Lq_entry

.Lq_skip_F:
	s_waitcnt lgkmcnt(0)
	s_barrier
	v_readlane_b32 s98, v251, 3
	v_readlane_b32 s99, v255, 29
	s_cmp_lt_u32 s98, 16
	s_cbranch_scc1 .Lwqd_skip_F
	s_sub_i32 s98, s98, 16
	s_mov_b32 s100, 0
	s_mov_b32 s101, 0
	s_cmp_eq_u32 s99, 0
	s_cselect_b32 s100, 0x5b0, s100
	s_cselect_b32 s101, 0x880, s101
	s_cmp_eq_u32 s99, 2
	s_cselect_b32 s100, 0x10d0, s100
	s_cselect_b32 s101, 0x1360, s101
	s_add_i32 s98, s98, s100
	s_mov_b32 s99, s101
	s_cmp_ge_u32 s98, s99
	s_cbranch_scc1 .Lwqd_skip_F
	s_movk_i32 s100, 240
	s_mov_b32 s101, 2
	v_writelane_b32 v117, s0, 0
	v_writelane_b32 v117, s1, 1
	v_writelane_b32 v117, s2, 2
	v_writelane_b32 v117, s3, 3
	v_writelane_b32 v117, s4, 4
	v_writelane_b32 v117, s5, 5
	v_writelane_b32 v117, s6, 6
	v_writelane_b32 v117, s7, 7
	v_writelane_b32 v117, s8, 8
	v_writelane_b32 v117, s9, 9
	v_writelane_b32 v117, s10, 10
	v_writelane_b32 v117, s11, 11
	v_writelane_b32 v117, s12, 12
	v_writelane_b32 v117, s13, 13
	v_writelane_b32 v117, s14, 14
	v_writelane_b32 v117, s15, 15
	v_writelane_b32 v117, s16, 16
	v_writelane_b32 v117, s17, 17
	v_writelane_b32 v117, s18, 18
	v_writelane_b32 v117, s19, 19
	v_writelane_b32 v117, s20, 20
	v_writelane_b32 v117, s21, 21
	v_writelane_b32 v117, s22, 22
	v_writelane_b32 v117, s23, 23
	v_writelane_b32 v117, s24, 24
	v_writelane_b32 v117, s25, 25
	v_writelane_b32 v117, s26, 26
	v_writelane_b32 v117, s27, 27
	v_writelane_b32 v117, s28, 28
	v_writelane_b32 v117, s29, 29
	v_writelane_b32 v117, s30, 30
	v_writelane_b32 v117, s31, 31
	v_writelane_b32 v117, s32, 32
	v_writelane_b32 v117, s33, 33
	v_writelane_b32 v117, s34, 34
	v_writelane_b32 v117, s35, 35
	v_writelane_b32 v117, s36, 36
	v_writelane_b32 v117, s37, 37
	v_writelane_b32 v117, s38, 38
	v_writelane_b32 v117, s39, 39
	v_writelane_b32 v117, s40, 40
	v_writelane_b32 v117, s41, 41
	v_writelane_b32 v117, s42, 42
	v_writelane_b32 v117, s43, 43
	v_writelane_b32 v117, s44, 44
	v_writelane_b32 v117, s45, 45
	v_writelane_b32 v117, s46, 46
	v_writelane_b32 v117, s47, 47
	v_writelane_b32 v117, s48, 48
	v_writelane_b32 v117, s49, 49
	v_writelane_b32 v117, s50, 50
	v_writelane_b32 v117, s51, 51
	v_writelane_b32 v117, s52, 52
	v_writelane_b32 v117, s53, 53
	v_writelane_b32 v117, s54, 54
	v_writelane_b32 v117, s55, 55
	v_writelane_b32 v117, s56, 56
	v_writelane_b32 v117, s57, 57
	v_writelane_b32 v117, s58, 58
	v_writelane_b32 v117, s59, 59
	v_writelane_b32 v117, s60, 60
	v_writelane_b32 v117, s61, 61
	v_writelane_b32 v117, s62, 62
	v_writelane_b32 v117, s63, 63
	v_writelane_b32 v118, s64, 0
	v_writelane_b32 v118, s65, 1
	v_writelane_b32 v118, s66, 2
	v_writelane_b32 v118, s67, 3
	v_writelane_b32 v118, s68, 4
	v_writelane_b32 v118, s69, 5
	v_writelane_b32 v118, s70, 6
	v_writelane_b32 v118, s71, 7
	v_writelane_b32 v118, s72, 8
	v_writelane_b32 v118, s73, 9
	v_writelane_b32 v118, s74, 10
	v_writelane_b32 v118, s75, 11
	v_writelane_b32 v118, s76, 12
	v_writelane_b32 v118, s77, 13
	v_writelane_b32 v118, s78, 14
	v_writelane_b32 v118, s79, 15
	v_writelane_b32 v118, s80, 16
	v_writelane_b32 v118, s81, 17
	v_writelane_b32 v118, s82, 18
	v_writelane_b32 v118, s83, 19
	v_writelane_b32 v118, s84, 20
	v_writelane_b32 v118, s85, 21
	v_writelane_b32 v118, s86, 22
	v_writelane_b32 v118, s87, 23
	v_writelane_b32 v118, s88, 24
	v_writelane_b32 v118, s89, 25
	v_writelane_b32 v118, s90, 26
	v_writelane_b32 v118, s91, 27
	v_writelane_b32 v118, s92, 28
	v_writelane_b32 v118, s93, 29
	v_writelane_b32 v118, s94, 30
	v_writelane_b32 v118, s95, 31
	v_writelane_b32 v118, s96, 32
	v_writelane_b32 v118, s97, 33
	v_mov_b32_e32 v100, v0
	v_mov_b32_e32 v101, v50
	v_mov_b32_e32 v102, v51
	v_mov_b32_e32 v103, v52
	v_mov_b32_e32 v104, v54
	v_mov_b32_e32 v105, v55
	v_mov_b32_e32 v106, v56
	v_mov_b32_e32 v107, v58
	v_mov_b32_e32 v108, v59
	v_mov_b32_e32 v109, v60
	v_mov_b32_e32 v110, v62
	v_mov_b32_e32 v111, v63
	v_mov_b32_e32 v112, v64
	v_mov_b32_e32 v113, v67
	v_mov_b32_e32 v114, v75
	v_mov_b32_e32 v115, v77
	s_branch .Lwqd_entry
